# combination: v10 + mLSTM-A/C V-load hoists + P0 MOD 2x unroll + P1 gather unroll
# speedup vs baseline: 1.0057x; 1.0057x over previous
.LBB0_106:
	v_ashrrev_i32_e32 v9, 1, v3
	v_and_b32_e32 v14, 4, v8
	v_mad_i64_i32 v[10:11], s[10:11], v9, s8, v[6:7]
	v_lshlrev_b32_e32 v4, 2, v14
	v_lshl_add_u64 v[10:11], v[10:11], 0, v[4:5]
	s_mov_b32 s10, 0x3000
	s_mov_b32 s11, 0
	v_lshl_add_u64 v[10:11], v[10:11], 0, s[10:11]
	s_mov_b32 s10, 0x602000
	global_load_dwordx4 v[112:115], v[10:11], off
	v_lshl_add_u64 v[10:11], v[10:11], 0, s[10:11]
	global_load_dwordx4 v[116:119], v[10:11], off
	v_lshl_add_u64 v[10:11], v[10:11], 0, s[10:11]
	global_load_dwordx4 v[120:123], v[10:11], off
	v_lshl_add_u64 v[10:11], v[10:11], 0, s[10:11]
	global_load_dwordx4 v[124:127], v[10:11], off
	v_lshl_add_u64 v[10:11], v[10:11], 0, s[10:11]
	global_load_dwordx4 v[128:131], v[10:11], off
	v_lshl_add_u64 v[10:11], v[10:11], 0, s[10:11]
	global_load_dwordx4 v[132:135], v[10:11], off
	v_lshl_add_u64 v[10:11], v[10:11], 0, s[10:11]
	global_load_dwordx4 v[136:139], v[10:11], off
	v_lshl_add_u64 v[10:11], v[10:11], 0, s[10:11]
	global_load_dwordx4 v[140:143], v[10:11], off
	v_lshlrev_b32_e32 v9, 2, v9
	v_lshlrev_b32_e32 v14, 13, v14
	v_add3_u32 v4, 0, v9, v14
	s_waitcnt vmcnt(7)
	ds_write2st64_b32 v4, v112, v113 offset1:32
	ds_write2st64_b32 v4, v114, v115 offset0:64 offset1:96
	v_add_u32_e32 v4, 0x400, v4
	s_waitcnt vmcnt(6)
	ds_write2st64_b32 v4, v116, v117 offset1:32
	ds_write2st64_b32 v4, v118, v119 offset0:64 offset1:96
	v_add_u32_e32 v4, 0x400, v4
	s_waitcnt vmcnt(5)
	ds_write2st64_b32 v4, v120, v121 offset1:32
	ds_write2st64_b32 v4, v122, v123 offset0:64 offset1:96
	v_add_u32_e32 v4, 0x400, v4
	s_waitcnt vmcnt(4)
	ds_write2st64_b32 v4, v124, v125 offset1:32
	ds_write2st64_b32 v4, v126, v127 offset0:64 offset1:96
	v_add_u32_e32 v4, 0x400, v4
	s_waitcnt vmcnt(3)
	ds_write2st64_b32 v4, v128, v129 offset1:32
	ds_write2st64_b32 v4, v130, v131 offset0:64 offset1:96
	v_add_u32_e32 v4, 0x400, v4
	s_waitcnt vmcnt(2)
	ds_write2st64_b32 v4, v132, v133 offset1:32
	ds_write2st64_b32 v4, v134, v135 offset0:64 offset1:96
	v_add_u32_e32 v4, 0x400, v4
	s_waitcnt vmcnt(1)
	ds_write2st64_b32 v4, v136, v137 offset1:32
	ds_write2st64_b32 v4, v138, v139 offset0:64 offset1:96
	v_add_u32_e32 v4, 0x400, v4
	s_waitcnt vmcnt(0)
	ds_write2st64_b32 v4, v140, v141 offset1:32
	ds_write2st64_b32 v4, v142, v143 offset0:64 offset1:96
	s_or_b64 exec, exec, s[6:7]

.LBB0_436:
	s_or_b64 exec, exec, s[64:65]
	v_readlane_b32 s64, v252, 12
	v_readlane_b32 s65, v252, 13
	s_lshl_b32 s66, s81, 9
	s_nop 3
	s_add_u32 s64, s64, s66
	s_addc_u32 s65, s65, 0
	v_lshlrev_b32_e32 v158, 2, v0
	v_and_b32_e32 v158, 0x1fc, v158
	v_mov_b32_e32 v159, 0
	v_lshl_add_u64 v[160:161], s[64:65], 0, v[158:159]
	v_ashrrev_i32_e32 v158, 3, v0
	v_and_b32_e32 v158, -16, v158
	v_add_u32_e32 v158, s82, v158
	v_mad_i64_i32 v[162:163], s[64:65], v158, s70, v[160:161]
	s_mov_b32 s66, 0x3000
	s_mov_b32 s67, 0
	global_load_dword v142, v[162:163], off offset:2048
	v_lshl_add_u64 v[162:163], v[162:163], 0, s[66:67]
	global_load_dword v143, v[162:163], off offset:2048
	v_lshl_add_u64 v[162:163], v[162:163], 0, s[66:67]
	global_load_dword v144, v[162:163], off offset:2048
	v_lshl_add_u64 v[162:163], v[162:163], 0, s[66:67]
	global_load_dword v145, v[162:163], off offset:2048
	v_lshl_add_u64 v[162:163], v[162:163], 0, s[66:67]
	global_load_dword v146, v[162:163], off offset:2048
	v_lshl_add_u64 v[162:163], v[162:163], 0, s[66:67]
	global_load_dword v147, v[162:163], off offset:2048
	v_lshl_add_u64 v[162:163], v[162:163], 0, s[66:67]
	global_load_dword v148, v[162:163], off offset:2048
	v_lshl_add_u64 v[162:163], v[162:163], 0, s[66:67]
	global_load_dword v149, v[162:163], off offset:2048
	v_lshl_add_u64 v[162:163], v[162:163], 0, s[66:67]
	global_load_dword v150, v[162:163], off offset:2048
	v_lshl_add_u64 v[162:163], v[162:163], 0, s[66:67]
	global_load_dword v151, v[162:163], off offset:2048
	v_lshl_add_u64 v[162:163], v[162:163], 0, s[66:67]
	global_load_dword v152, v[162:163], off offset:2048
	v_lshl_add_u64 v[162:163], v[162:163], 0, s[66:67]
	global_load_dword v153, v[162:163], off offset:2048
	v_lshl_add_u64 v[162:163], v[162:163], 0, s[66:67]
	global_load_dword v154, v[162:163], off offset:2048
	v_lshl_add_u64 v[162:163], v[162:163], 0, s[66:67]
	global_load_dword v155, v[162:163], off offset:2048
	v_lshl_add_u64 v[162:163], v[162:163], 0, s[66:67]
	global_load_dword v156, v[162:163], off offset:2048
	v_lshl_add_u64 v[162:163], v[162:163], 0, s[66:67]
	global_load_dword v157, v[162:163], off offset:2048
	s_waitcnt vmcnt(0)
	v_lshlrev_b32_e32 v14, 16, v24
	v_and_b32_e32 v15, 0xffff0000, v24
	v_lshlrev_b32_e32 v22, 16, v23
	v_and_b32_e32 v23, 0xffff0000, v23
	v_pk_fma_f32 v[14:15], v[8:9], v[14:15], v[12:13]
	v_lshlrev_b32_e32 v20, 16, v21
	v_and_b32_e32 v21, 0xffff0000, v21
	v_pk_fma_f32 v[14:15], v[4:5], v[22:23], v[14:15]
	v_lshlrev_b32_e32 v18, 16, v19
	v_and_b32_e32 v19, 0xffff0000, v19
	v_pk_fma_f32 v[14:15], v[6:7], v[20:21], v[14:15]
	v_and_b32_e32 v29, 0xfe, v17
	v_pk_fma_f32 v[24:25], v[10:11], v[18:19], v[14:15]
	s_lshl_b32 s58, s8, 1
	v_mul_f32_e32 v14, 0xbfb8aa3b, v24
	v_exp_f32_e32 v17, v14
	v_mul_f32_e32 v14, 0xbfb8aa3b, v25
	v_exp_f32_e32 v31, v14
	s_add_u32 s8, s16, s58
	v_add_f32_e32 v17, 1.0, v17
	v_rcp_f32_e32 v46, v17
	v_add_f32_e32 v17, 1.0, v31
	v_rcp_f32_e32 v47, v17
	s_addc_u32 s9, s17, 0
	v_lshlrev_b32_e32 v66, 1, v16
	s_add_u32 s64, s6, s58
	v_cmp_lt_u32_e32 vcc, s72, v29
	v_lshl_add_u64 v[14:15], s[8:9], 0, v[66:67]
	v_mad_u32_u24 v31, v16, s73, 0
	s_addc_u32 s65, s7, 0
	v_pk_mul_f32 v[24:25], v[24:25], v[46:47]
	s_and_saveexec_b64 s[8:9], vcc
	s_xor_b64 s[66:67], exec, s[8:9]
	s_cbranch_execz .LBB0_438
	v_pk_mul_f32 v[16:17], v[24:25], s[60:61] op_sel_hi:[1,0]
	s_nop 0
	v_bfe_u32 v24, v16, 16, 1
	v_add3_u32 v24, v16, v24, s75
	v_bfe_u32 v25, v17, 16, 1
	v_lshrrev_b32_e32 v16, 16, v24
	v_add3_u32 v25, v17, v25, s75
	v_and_or_b32 v46, v25, s71, v16
	v_add_u32_e32 v16, s82, v2
	v_ashrrev_i32_e32 v17, 31, v16
	v_lshlrev_b64 v[16:17], 10, v[16:17]
	v_lshl_add_u64 v[16:17], v[14:15], 0, v[16:17]
	global_store_dword v[16:17], v46, off
	v_lshl_add_u32 v16, v2, 1, v31
	ds_write_b16_d16_hi v16, v24 offset:1024
	ds_write_b16_d16_hi v16, v25 offset:1168

.LBB0_504:
	v_lshlrev_b32_e32 v1, 1, v28
	v_mad_u32_u24 v9, v29, s73, 0
	v_and_b32_e32 v1, 0xffffffe0, v1
	v_add_u32_e32 v1, v9, v1
	v_add_u32_e32 v3, 0x4c00, v1
	v_add_u32_e32 v4, 0x4c1e, v1
	v_cmp_ge_u32_e32 vcc, v4, v3
	v_add_u32_e32 v3, 0x4c90, v1
	v_add_u32_e32 v1, 0x4cae, v1
	v_cmp_ge_u32_e64 s[2:3], v1, v3
	s_and_b64 s[2:3], vcc, s[2:3]
	s_waitcnt lgkmcnt(0)
	s_barrier
	s_and_saveexec_b64 s[8:9], s[2:3]
	s_xor_b64 s[2:3], exec, s[8:9]
	s_cbranch_execz .LBB0_507
	s_lshl_b32 s8, s81, 9
	v_readlane_b32 s64, v252, 12
	v_add_u32_e32 v6, 2, v2
	v_add_u32_e32 v10, 4, v2
	v_add_u32_e32 v14, 6, v2
	v_readlane_b32 s65, v252, 13
	s_add_u32 s64, s64, s8
	v_add_u32_e32 v4, s82, v2
	v_add_u32_e32 v8, s82, v6
	v_add_u32_e32 v12, s82, v10
	v_add_u32_e32 v16, s82, v14
	s_addc_u32 s65, s65, 0
	v_lshlrev_b32_e32 v66, 1, v29
	v_mov_b32_e32 v1, v4
	v_mov_b32_e32 v3, v8
	v_mov_b32_e32 v5, v12
	v_mov_b32_e32 v7, v16
	s_mov_b32 s8, 1
	v_lshl_add_u64 v[18:19], s[64:65], 0, v[66:67]
	s_mov_b32 s9, 0
	s_mov_b32 s58, 16
	v_add_u32_e32 v13, s8, v1
	v_add_u32_e32 v15, s9, v4
	v_add_u32_e32 v30, s8, v3
	v_add_u32_e32 v24, s9, v8
	v_add_u32_e32 v34, s8, v5
	v_add_u32_e32 v32, s9, v12
	v_add_u32_e32 v38, s8, v7
	v_add_u32_e32 v36, s9, v16
	v_mad_i64_i32 v[22:23], s[64:65], v13, s70, v[18:19]
	v_mad_i64_i32 v[20:21], s[64:65], v15, s70, v[18:19]
	v_mad_i64_i32 v[24:25], s[64:65], v24, s70, v[18:19]
	v_mad_i64_i32 v[30:31], s[64:65], v30, s70, v[18:19]
	v_mad_i64_i32 v[32:33], s[64:65], v32, s70, v[18:19]
	v_mad_i64_i32 v[34:35], s[64:65], v34, s70, v[18:19]
	v_mad_i64_i32 v[36:37], s[64:65], v36, s70, v[18:19]
	v_mad_i64_i32 v[38:39], s[64:65], v38, s70, v[18:19]
	v_mov_b32_e32 v13, v143
	v_mov_b32_e32 v15, v142
	v_mov_b32_e32 v42, v145
	v_mov_b32_e32 v43, v144
	v_mov_b32_e32 v44, v147
	v_mov_b32_e32 v45, v146
	v_mov_b32_e32 v46, v149
	v_mov_b32_e32 v48, v148
	v_add_u32_e32 v11, s9, v2
	v_add_u32_e32 v17, s9, v6
	v_add_u32_e32 v40, s9, v10
	v_add_u32_e32 v41, s9, v14
	v_lshl_add_u32 v20, v11, 2, 0
	v_lshl_add_u32 v22, v17, 2, 0
	v_lshl_add_u32 v24, v40, 2, 0
	v_lshl_add_u32 v30, v40, 1, v9
	v_lshl_add_u32 v31, v41, 2, 0
	ds_read_b64 v[20:21], v20
	ds_read_b64 v[22:23], v22
	ds_read_b64 v[24:25], v24
	v_add_u32_e32 v49, 0x4c00, v30
	ds_read_b64 v[30:31], v31
	v_lshl_add_u32 v32, v41, 1, v9
	v_add_u32_e32 v50, 0x4c00, v32
	s_add_i32 s9, s9, 8
	s_add_i32 s8, s8, 8
	s_add_i32 s58, s58, -8
	v_lshl_add_u32 v11, v11, 1, v9
	v_lshl_add_u32 v17, v17, 1, v9
	s_cmp_lg_u32 s58, 0
	v_add_u32_e32 v11, 0x4c00, v11
	v_add_u32_e32 v17, 0x4c00, v17
	v_lshlrev_b32_e32 v33, 16, v13
	v_lshlrev_b32_e32 v32, 16, v15
	v_and_b32_e32 v35, 0xffff0000, v13
	v_and_b32_e32 v34, 0xffff0000, v15
	v_lshlrev_b32_e32 v37, 16, v42
	v_lshlrev_b32_e32 v36, 16, v43
	v_and_b32_e32 v39, 0xffff0000, v42
	v_and_b32_e32 v38, 0xffff0000, v43
	v_lshlrev_b32_e32 v41, 16, v44
	v_lshlrev_b32_e32 v40, 16, v45
	v_and_b32_e32 v43, 0xffff0000, v44
	v_and_b32_e32 v42, 0xffff0000, v45
	v_lshlrev_b32_e32 v45, 16, v46
	v_lshlrev_b32_e32 v44, 16, v48
	v_and_b32_e32 v47, 0xffff0000, v46
	v_and_b32_e32 v46, 0xffff0000, v48
	s_waitcnt lgkmcnt(3)
	v_pk_mul_f32 v[32:33], v[20:21], v[32:33]
	v_pk_mul_f32 v[20:21], v[20:21], v[34:35]
	s_waitcnt lgkmcnt(2)
	v_pk_mul_f32 v[34:35], v[22:23], v[36:37]
	v_pk_mul_f32 v[22:23], v[22:23], v[38:39]
	s_waitcnt lgkmcnt(1)
	v_pk_mul_f32 v[36:37], v[24:25], v[40:41]
	v_pk_mul_f32 v[24:25], v[24:25], v[42:43]
	s_waitcnt lgkmcnt(0)
	v_pk_mul_f32 v[38:39], v[30:31], v[44:45]
	v_pk_mul_f32 v[30:31], v[30:31], v[46:47]
	v_and_b32_sdwa v13, v33, v70 dst_sel:DWORD dst_unused:UNUSED_PAD src0_sel:WORD_1 src1_sel:DWORD
	v_and_b32_sdwa v15, v32, v70 dst_sel:DWORD dst_unused:UNUSED_PAD src0_sel:WORD_1 src1_sel:DWORD
	v_and_b32_sdwa v40, v21, v70 dst_sel:DWORD dst_unused:UNUSED_PAD src0_sel:WORD_1 src1_sel:DWORD
	v_and_b32_sdwa v41, v20, v70 dst_sel:DWORD dst_unused:UNUSED_PAD src0_sel:WORD_1 src1_sel:DWORD
	v_and_b32_sdwa v42, v35, v70 dst_sel:DWORD dst_unused:UNUSED_PAD src0_sel:WORD_1 src1_sel:DWORD
	v_and_b32_sdwa v43, v34, v70 dst_sel:DWORD dst_unused:UNUSED_PAD src0_sel:WORD_1 src1_sel:DWORD
	v_and_b32_sdwa v44, v23, v70 dst_sel:DWORD dst_unused:UNUSED_PAD src0_sel:WORD_1 src1_sel:DWORD
	v_and_b32_sdwa v45, v22, v70 dst_sel:DWORD dst_unused:UNUSED_PAD src0_sel:WORD_1 src1_sel:DWORD
	v_and_b32_sdwa v46, v37, v70 dst_sel:DWORD dst_unused:UNUSED_PAD src0_sel:WORD_1 src1_sel:DWORD
	v_and_b32_sdwa v47, v36, v70 dst_sel:DWORD dst_unused:UNUSED_PAD src0_sel:WORD_1 src1_sel:DWORD
	v_and_b32_sdwa v48, v25, v70 dst_sel:DWORD dst_unused:UNUSED_PAD src0_sel:WORD_1 src1_sel:DWORD
	v_and_b32_sdwa v51, v24, v70 dst_sel:DWORD dst_unused:UNUSED_PAD src0_sel:WORD_1 src1_sel:DWORD
	v_and_b32_sdwa v52, v39, v70 dst_sel:DWORD dst_unused:UNUSED_PAD src0_sel:WORD_1 src1_sel:DWORD
	v_and_b32_sdwa v53, v38, v70 dst_sel:DWORD dst_unused:UNUSED_PAD src0_sel:WORD_1 src1_sel:DWORD
	v_and_b32_sdwa v54, v31, v70 dst_sel:DWORD dst_unused:UNUSED_PAD src0_sel:WORD_1 src1_sel:DWORD
	v_and_b32_sdwa v55, v30, v70 dst_sel:DWORD dst_unused:UNUSED_PAD src0_sel:WORD_1 src1_sel:DWORD
	v_add3_u32 v15, v32, v15, s75
	v_add3_u32 v13, v33, v13, s75
	v_add3_u32 v20, v20, v41, s75
	v_add3_u32 v21, v21, v40, s75
	v_add3_u32 v32, v34, v43, s75
	v_add3_u32 v33, v35, v42, s75
	v_add3_u32 v22, v22, v45, s75
	v_add3_u32 v23, v23, v44, s75
	v_add3_u32 v34, v36, v47, s75
	v_add3_u32 v35, v37, v46, s75
	v_add3_u32 v24, v24, v51, s75
	v_add3_u32 v25, v25, v48, s75
	v_add3_u32 v36, v38, v53, s75
	v_add3_u32 v37, v39, v52, s75
	v_add3_u32 v30, v30, v55, s75
	v_add3_u32 v31, v31, v54, s75
	v_perm_b32 v13, v13, v15, s80
	v_perm_b32 v15, v21, v20, s80
	v_perm_b32 v20, v33, v32, s80
	v_perm_b32 v21, v23, v22, s80
	v_perm_b32 v22, v35, v34, s80
	v_perm_b32 v23, v25, v24, s80
	v_perm_b32 v24, v37, v36, s80
	v_perm_b32 v25, v31, v30, s80
	ds_write2_b32 v11, v13, v15 offset1:36
	ds_write2_b32 v17, v20, v21 offset1:36
	ds_write2_b32 v49, v22, v23 offset1:36
	ds_write2_b32 v50, v24, v25 offset1:36
	v_add_u32_e32 v13, s8, v1
	v_add_u32_e32 v15, s9, v4
	v_add_u32_e32 v30, s8, v3
	v_add_u32_e32 v24, s9, v8
	v_add_u32_e32 v34, s8, v5
	v_add_u32_e32 v32, s9, v12
	v_add_u32_e32 v38, s8, v7
	v_add_u32_e32 v36, s9, v16
	v_mad_i64_i32 v[22:23], s[64:65], v13, s70, v[18:19]
	v_mad_i64_i32 v[20:21], s[64:65], v15, s70, v[18:19]
	v_mad_i64_i32 v[24:25], s[64:65], v24, s70, v[18:19]
	v_mad_i64_i32 v[30:31], s[64:65], v30, s70, v[18:19]
	v_mad_i64_i32 v[32:33], s[64:65], v32, s70, v[18:19]
	v_mad_i64_i32 v[34:35], s[64:65], v34, s70, v[18:19]
	v_mad_i64_i32 v[36:37], s[64:65], v36, s70, v[18:19]
	v_mad_i64_i32 v[38:39], s[64:65], v38, s70, v[18:19]
	v_mov_b32_e32 v13, v151
	v_mov_b32_e32 v15, v150
	v_mov_b32_e32 v42, v153
	v_mov_b32_e32 v43, v152
	v_mov_b32_e32 v44, v155
	v_mov_b32_e32 v45, v154
	v_mov_b32_e32 v46, v157
	v_mov_b32_e32 v48, v156
	v_add_u32_e32 v11, s9, v2
	v_add_u32_e32 v17, s9, v6
	v_add_u32_e32 v40, s9, v10
	v_add_u32_e32 v41, s9, v14
	v_lshl_add_u32 v20, v11, 2, 0
	v_lshl_add_u32 v22, v17, 2, 0
	v_lshl_add_u32 v24, v40, 2, 0
	v_lshl_add_u32 v30, v40, 1, v9
	v_lshl_add_u32 v31, v41, 2, 0
	ds_read_b64 v[20:21], v20
	ds_read_b64 v[22:23], v22
	ds_read_b64 v[24:25], v24
	v_add_u32_e32 v49, 0x4c00, v30
	ds_read_b64 v[30:31], v31
	v_lshl_add_u32 v32, v41, 1, v9
	v_add_u32_e32 v50, 0x4c00, v32
	s_add_i32 s9, s9, 8
	s_add_i32 s8, s8, 8
	s_add_i32 s58, s58, -8
	v_lshl_add_u32 v11, v11, 1, v9
	v_lshl_add_u32 v17, v17, 1, v9
	s_cmp_lg_u32 s58, 0
	v_add_u32_e32 v11, 0x4c00, v11
	v_add_u32_e32 v17, 0x4c00, v17
	v_lshlrev_b32_e32 v33, 16, v13
	v_lshlrev_b32_e32 v32, 16, v15
	v_and_b32_e32 v35, 0xffff0000, v13
	v_and_b32_e32 v34, 0xffff0000, v15
	v_lshlrev_b32_e32 v37, 16, v42
	v_lshlrev_b32_e32 v36, 16, v43
	v_and_b32_e32 v39, 0xffff0000, v42
	v_and_b32_e32 v38, 0xffff0000, v43
	v_lshlrev_b32_e32 v41, 16, v44
	v_lshlrev_b32_e32 v40, 16, v45
	v_and_b32_e32 v43, 0xffff0000, v44
	v_and_b32_e32 v42, 0xffff0000, v45
	v_lshlrev_b32_e32 v45, 16, v46
	v_lshlrev_b32_e32 v44, 16, v48
	v_and_b32_e32 v47, 0xffff0000, v46
	v_and_b32_e32 v46, 0xffff0000, v48
	s_waitcnt lgkmcnt(3)
	v_pk_mul_f32 v[32:33], v[20:21], v[32:33]
	v_pk_mul_f32 v[20:21], v[20:21], v[34:35]
	s_waitcnt lgkmcnt(2)
	v_pk_mul_f32 v[34:35], v[22:23], v[36:37]
	v_pk_mul_f32 v[22:23], v[22:23], v[38:39]
	s_waitcnt lgkmcnt(1)
	v_pk_mul_f32 v[36:37], v[24:25], v[40:41]
	v_pk_mul_f32 v[24:25], v[24:25], v[42:43]
	s_waitcnt lgkmcnt(0)
	v_pk_mul_f32 v[38:39], v[30:31], v[44:45]
	v_pk_mul_f32 v[30:31], v[30:31], v[46:47]
	v_and_b32_sdwa v13, v33, v70 dst_sel:DWORD dst_unused:UNUSED_PAD src0_sel:WORD_1 src1_sel:DWORD
	v_and_b32_sdwa v15, v32, v70 dst_sel:DWORD dst_unused:UNUSED_PAD src0_sel:WORD_1 src1_sel:DWORD
	v_and_b32_sdwa v40, v21, v70 dst_sel:DWORD dst_unused:UNUSED_PAD src0_sel:WORD_1 src1_sel:DWORD
	v_and_b32_sdwa v41, v20, v70 dst_sel:DWORD dst_unused:UNUSED_PAD src0_sel:WORD_1 src1_sel:DWORD
	v_and_b32_sdwa v42, v35, v70 dst_sel:DWORD dst_unused:UNUSED_PAD src0_sel:WORD_1 src1_sel:DWORD
	v_and_b32_sdwa v43, v34, v70 dst_sel:DWORD dst_unused:UNUSED_PAD src0_sel:WORD_1 src1_sel:DWORD
	v_and_b32_sdwa v44, v23, v70 dst_sel:DWORD dst_unused:UNUSED_PAD src0_sel:WORD_1 src1_sel:DWORD
	v_and_b32_sdwa v45, v22, v70 dst_sel:DWORD dst_unused:UNUSED_PAD src0_sel:WORD_1 src1_sel:DWORD
	v_and_b32_sdwa v46, v37, v70 dst_sel:DWORD dst_unused:UNUSED_PAD src0_sel:WORD_1 src1_sel:DWORD
	v_and_b32_sdwa v47, v36, v70 dst_sel:DWORD dst_unused:UNUSED_PAD src0_sel:WORD_1 src1_sel:DWORD
	v_and_b32_sdwa v48, v25, v70 dst_sel:DWORD dst_unused:UNUSED_PAD src0_sel:WORD_1 src1_sel:DWORD
	v_and_b32_sdwa v51, v24, v70 dst_sel:DWORD dst_unused:UNUSED_PAD src0_sel:WORD_1 src1_sel:DWORD
	v_and_b32_sdwa v52, v39, v70 dst_sel:DWORD dst_unused:UNUSED_PAD src0_sel:WORD_1 src1_sel:DWORD
	v_and_b32_sdwa v53, v38, v70 dst_sel:DWORD dst_unused:UNUSED_PAD src0_sel:WORD_1 src1_sel:DWORD
	v_and_b32_sdwa v54, v31, v70 dst_sel:DWORD dst_unused:UNUSED_PAD src0_sel:WORD_1 src1_sel:DWORD
	v_and_b32_sdwa v55, v30, v70 dst_sel:DWORD dst_unused:UNUSED_PAD src0_sel:WORD_1 src1_sel:DWORD
	v_add3_u32 v15, v32, v15, s75
	v_add3_u32 v13, v33, v13, s75
	v_add3_u32 v20, v20, v41, s75
	v_add3_u32 v21, v21, v40, s75
	v_add3_u32 v32, v34, v43, s75
	v_add3_u32 v33, v35, v42, s75
	v_add3_u32 v22, v22, v45, s75
	v_add3_u32 v23, v23, v44, s75
	v_add3_u32 v34, v36, v47, s75
	v_add3_u32 v35, v37, v46, s75
	v_add3_u32 v24, v24, v51, s75
	v_add3_u32 v25, v25, v48, s75
	v_add3_u32 v36, v38, v53, s75
	v_add3_u32 v37, v39, v52, s75
	v_add3_u32 v30, v30, v55, s75
	v_add3_u32 v31, v31, v54, s75
	v_perm_b32 v13, v13, v15, s80
	v_perm_b32 v15, v21, v20, s80
	v_perm_b32 v20, v33, v32, s80
	v_perm_b32 v21, v23, v22, s80
	v_perm_b32 v22, v35, v34, s80
	v_perm_b32 v23, v25, v24, s80
	v_perm_b32 v24, v37, v36, s80
	v_perm_b32 v25, v31, v30, s80
	ds_write2_b32 v11, v13, v15 offset1:36
	ds_write2_b32 v17, v20, v21 offset1:36
	ds_write2_b32 v49, v22, v23 offset1:36
	ds_write2_b32 v50, v24, v25 offset1:36
